# baseline (speedup 1.0000x reference)
.LBB4_25:
	s_or_b64 exec, exec, s[4:5]
	v_and_b32_e32 v0, 15, v0
	s_movk_i32 s0, 0x90
	v_mad_u32_u24 v1, v0, s0, v72
	s_waitcnt lgkmcnt(0)
	s_barrier
	ds_read_b128 v[94:97], v1 offset:8256
	ds_read_b128 v[98:101], v1 offset:8320
	s_cmp_lg_u64 s[6:7], 0
	s_cbranch_scc1 .Lmy_r2_w0
	s_waitcnt vmcnt(4) lgkmcnt(1)
	v_mfma_f32_16x16x32_f16 a[0:3], v[94:97], v[6:9], 0
	v_lshlrev_b32_e32 v0, 2, v0
	s_movk_i32 s0, 0x810
	v_lshl_or_b32 v0, s16, 7, v0
	s_waitcnt vmcnt(3)
	v_mfma_f32_16x16x32_f16 a[4:7], v[94:97], v[38:41], 0
	v_mad_u32_u24 v0, v82, s0, v0
	s_movk_i32 s0, 0x204
	s_waitcnt lgkmcnt(0)
	v_mfma_f32_16x16x32_f16 a[0:3], v[98:101], v[90:93], a[0:3]
	v_mad_u32_u24 v38, v84, s0, v85
	s_waitcnt vmcnt(2)
	v_cvt_f32_f16_sdwa v1, v46 dst_sel:DWORD dst_unused:UNUSED_PAD src0_sel:WORD_1
	v_cvt_f32_f16_sdwa v9, v47 dst_sel:DWORD dst_unused:UNUSED_PAD src0_sel:WORD_1
	v_mfma_f32_16x16x32_f16 a[4:7], v[98:101], v[104:107], a[4:7]
	s_branch .Lmy_r2_join
.Lmy_r2_w0:
	s_waitcnt vmcnt(19) lgkmcnt(1)
	v_mfma_f32_16x16x32_f16 a[0:3], v[94:97], v[6:9], 0
	v_lshlrev_b32_e32 v0, 2, v0
	s_movk_i32 s0, 0x810
	v_lshl_or_b32 v0, s16, 7, v0
	s_waitcnt vmcnt(18)
	v_mfma_f32_16x16x32_f16 a[4:7], v[94:97], v[38:41], 0
	v_mad_u32_u24 v0, v82, s0, v0
	s_movk_i32 s0, 0x204
	s_waitcnt lgkmcnt(0)
	v_mfma_f32_16x16x32_f16 a[0:3], v[98:101], v[90:93], a[0:3]
	v_mad_u32_u24 v38, v84, s0, v85
	s_waitcnt vmcnt(17)
	v_cvt_f32_f16_sdwa v1, v46 dst_sel:DWORD dst_unused:UNUSED_PAD src0_sel:WORD_1
	v_cvt_f32_f16_sdwa v9, v47 dst_sel:DWORD dst_unused:UNUSED_PAD src0_sel:WORD_1
	v_mfma_f32_16x16x32_f16 a[4:7], v[98:101], v[104:107], a[4:7]
.Lmy_r2_join:
	s_nop 2
	ds_write_b32 v0, a0
	ds_write_b32 v0, a1 offset:516
	ds_write_b32 v0, a2 offset:1032
	ds_write_b32 v0, a3 offset:1548
	s_nop 0
	ds_write_b32 v0, a4 offset:64
	ds_write_b32 v0, a5 offset:580
	ds_write_b32 v0, a6 offset:1096
	ds_write_b32 v0, a7 offset:1612
	s_waitcnt lgkmcnt(0)
	s_barrier
	ds_read2_b32 v[6:7], v38 offset1:1
	v_cvt_f32_f16_e32 v0, v46
	v_cvt_f32_f16_e32 v8, v47
	ds_read2_b32 v[22:23], v38 offset0:2 offset1:3
	ds_read2_b32 v[24:25], v38 offset0:4 offset1:5
	ds_read2_b32 v[38:39], v38 offset0:6 offset1:7
	v_mov_b32_e32 v71, 0
	s_waitcnt vmcnt(0) lgkmcnt(3)
	v_pk_fma_f32 v[0:1], v[50:51], v[6:7], v[0:1]
	s_andn2_b64 vcc, exec, s[6:7]
	v_cvt_pk_f16_f32 v6, v0, v1
	s_waitcnt lgkmcnt(2)
	v_pk_fma_f32 v[0:1], v[52:53], v[22:23], v[8:9]
	v_cvt_f32_f16_sdwa v9, v48 dst_sel:DWORD dst_unused:UNUSED_PAD src0_sel:WORD_1
	v_cvt_f32_f16_e32 v8, v48
	v_cvt_f32_f16_sdwa v23, v49 dst_sel:DWORD dst_unused:UNUSED_PAD src0_sel:WORD_1
	v_cvt_f32_f16_e32 v22, v49
	v_cvt_pk_f16_f32 v7, v0, v1
	s_waitcnt lgkmcnt(1)
	v_pk_fma_f32 v[0:1], v[42:43], v[24:25], v[8:9]
	s_nop 0
	v_cvt_pk_f16_f32 v8, v0, v1
	s_waitcnt lgkmcnt(0)
	v_pk_fma_f32 v[0:1], v[44:45], v[38:39], v[22:23]
	s_nop 0
	v_cvt_pk_f16_f32 v9, v0, v1
	v_lshl_add_u64 v[0:1], v[78:79], 1, s[2:3]
	v_lshl_add_u64 v[0:1], v[0:1], 0, v[70:71]
	global_store_dwordx4 v[0:1], v[6:9], off
	s_cbranch_vccnz .LBB4_27
	s_nop 0
	v_add_f32_e32 v6, v73, v75
	v_add_f32_e32 v6, v6, v83
	v_add_f32_e32 v22, v6, v86
	v_div_scale_f32 v23, s[0:1], v22, v22, 1.0
	v_rcp_f32_e32 v24, v23
	v_pk_add_f32 v[6:7], v[12:13], v[60:61]
	v_pk_add_f32 v[0:1], v[10:11], v[58:59]
	v_pk_add_f32 v[8:9], v[34:35], v[54:55]
	v_fma_f32 v12, -v23, v24, 1.0
	v_fmac_f32_e32 v24, v12, v24
	v_div_scale_f32 v12, vcc, 1.0, v22, 1.0
	v_mul_f32_e32 v13, v12, v24
	v_fma_f32 v25, -v23, v13, v12
	v_fmac_f32_e32 v13, v25, v24
	v_fma_f32 v12, -v23, v13, v12
	v_div_fmas_f32 v12, v12, v24, v13
	v_div_fixup_f32 v12, v12, v22, 1.0
	v_cvt_f32_f16_sdwa v23, v2 dst_sel:DWORD dst_unused:UNUSED_PAD src0_sel:WORD_1
	v_cvt_f32_f16_e32 v22, v2
	v_pk_add_f32 v[0:1], v[0:1], v[14:15]
	v_cvt_f32_f16_sdwa v15, v3 dst_sel:DWORD dst_unused:UNUSED_PAD src0_sel:WORD_1
	v_cvt_f32_f16_e32 v14, v3
	v_pk_add_f32 v[2:3], v[6:7], v[16:17]
	v_pk_add_f32 v[0:1], v[0:1], v[62:63]
	v_pk_add_f32 v[2:3], v[2:3], v[64:65]
	v_pk_mul_f32 v[0:1], v[26:27], v[0:1]
	v_pk_mul_f32 v[2:3], v[28:29], v[2:3]
	v_pk_fma_f32 v[0:1], v[0:1], v[12:13], v[22:23] op_sel_hi:[1,0,1]
	v_pk_fma_f32 v[2:3], v[2:3], v[12:13], v[14:15] op_sel_hi:[1,0,1]
	v_cvt_pk_f16_f32 v0, v0, v1
	v_cvt_pk_f16_f32 v1, v2, v3
	v_cvt_f32_f16_sdwa v3, v4 dst_sel:DWORD dst_unused:UNUSED_PAD src0_sel:WORD_1
	v_cvt_f32_f16_e32 v2, v4
	v_pk_add_f32 v[6:7], v[8:9], v[18:19]
	v_pk_add_f32 v[10:11], v[36:37], v[56:57]
	v_pk_add_f32 v[6:7], v[6:7], v[66:67]
	s_movk_i32 s0, 0x140
	v_pk_mul_f32 v[6:7], v[30:31], v[6:7]
	v_mov_b32_e32 v75, v71
	v_pk_fma_f32 v[2:3], v[6:7], v[12:13], v[2:3] op_sel_hi:[1,0,1]
	v_cvt_f32_f16_sdwa v7, v5 dst_sel:DWORD dst_unused:UNUSED_PAD src0_sel:WORD_1
	v_cvt_f32_f16_e32 v6, v5
	v_pk_add_f32 v[4:5], v[10:11], v[20:21]
	v_cvt_pk_f16_f32 v2, v2, v3
	v_pk_add_f32 v[4:5], v[4:5], v[68:69]
	s_nop 0
	v_pk_mul_f32 v[4:5], v[32:33], v[4:5]
	s_nop 0
	v_pk_fma_f32 v[4:5], v[4:5], v[12:13], v[6:7] op_sel_hi:[1,0,1]
	s_nop 0
	v_cvt_pk_f16_f32 v3, v4, v5
	v_mov_b64_e32 v[4:5], s[2:3]
	v_mad_u64_u32 v[4:5], s[0:1], v76, s0, v[4:5]
	v_lshl_add_u64 v[4:5], v[4:5], 0, v[74:75]
	global_store_dwordx4 v[4:5], v[0:3], off offset:256
